# row pass 2 (combine): prefetch wait ladder moved to the rare modulation-reload path, single drain before the stores
# speedup vs baseline: 1.0053x; 1.0053x over previous
; #define RP_UNPK(V_, H_) ((H_) ? (f32x4){bflo((V_)[2]), bfhi((V_)[2]), bflo((V_)[3]), bfhi((V_)[3])} : (f32x4){bflo((V_)[0]), bfhi((V_)[0]), bflo((V_)[1]), bfhi((V_)[1])})
; template <int MODE, bool FIRSTX>
; __device__ __forceinline__ void row_pass(Frame& F, int layer, bool final_out, int row0) {
;     ...
;         for (int q = 0; q < 4; ++q) v[q] = FIRSTX ? xf[q] : RP_UNPK(xb[q >> 1], q & 1);
;         if (MODE != 0) {
; #pragma unroll
;             for (int q = 0; q < 4; ++q) { f32x4 y = (f32x4){0.f, 0.f, 0.f, 0.f};
; #pragma unroll
;                 for (int k = 0; k < NY; ++k) { if (MODE == 2) { const unsigned w8 = yb[k][q >> 1][q & 1]; const f32x2 lo = __builtin_amdgcn_cvt_pk_f32_fp8((int)w8, false), hi = __builtin_amdgcn_cvt_pk_f32_fp8((int)w8, true); y += (f32x4){lo.x, lo.y, hi.x, hi.y}; }
;                                                 else y += RP_UNPK(yb[k][q >> 1], q & 1); }
;                 if (MODE == 2) y = y * (1.0f / YK8_SCALE);
;                 v[q] = v[q] * DN_ALPHA + gt[q] * y; }
;             float s = 0.f;
; #pragma unroll
;             for (int q = 0; q < 4; ++q) s += (v[q][0] + v[q][1]) + (v[q][2] + v[q][3]);
;             const float mean = wave_sum(s) * (1.0f / DM); float qq = 0.f;
.LBB0_1209:
	s_waitcnt vmcnt(0)
	s_mov_b32 s8, s20
.LBB0_1210:
	v_lshlrev_b32_e32 v154, 16, v96
	v_and_b32_e32 v155, 0xffff0000, v96
	v_lshlrev_b32_e32 v156, 16, v97
	v_and_b32_e32 v157, 0xffff0000, v97
	v_lshlrev_b32_e32 v158, 16, v90
	v_and_b32_e32 v159, 0xffff0000, v90
	v_lshlrev_b32_e32 v160, 16, v91
	v_and_b32_e32 v161, 0xffff0000, v91
	v_lshlrev_b32_e32 v96, 16, v92
	v_and_b32_e32 v97, 0xffff0000, v92
	v_lshlrev_b32_e32 v150, 16, v93
	v_and_b32_e32 v151, 0xffff0000, v93
	v_cvt_pk_f32_fp8_e32 v[90:91], v142
	v_cvt_pk_f32_fp8_sdwa v[92:93], v142 src0_sel:WORD_1
	v_cvt_pk_f32_fp8_e32 v[162:163], v140
	v_cvt_pk_f32_fp8_sdwa v[164:165], v140 src0_sel:WORD_1
	v_pk_add_f32 v[90:91], v[90:91], 0 op_sel_hi:[1,0]
	v_pk_add_f32 v[92:93], v[92:93], 0 op_sel_hi:[1,0]
	v_pk_add_f32 v[90:91], v[90:91], v[162:163]
	v_pk_add_f32 v[92:93], v[92:93], v[164:165]
	v_cvt_pk_f32_fp8_e32 v[162:163], v144
	v_cvt_pk_f32_fp8_sdwa v[164:165], v144 src0_sel:WORD_1
	v_lshlrev_b32_e32 v152, 16, v94
	v_and_b32_e32 v153, 0xffff0000, v94
	v_pk_add_f32 v[90:91], v[90:91], v[162:163]
	v_pk_add_f32 v[92:93], v[92:93], v[164:165]
	v_cvt_pk_f32_fp8_e32 v[162:163], v148
	v_cvt_pk_f32_fp8_sdwa v[164:165], v148 src0_sel:WORD_1
	v_lshlrev_b32_e32 v94, 16, v95
	v_and_b32_e32 v95, 0xffff0000, v95
	v_pk_add_f32 v[90:91], v[90:91], v[162:163]
	v_pk_add_f32 v[92:93], v[92:93], v[164:165]
	v_pk_mul_f32 v[90:91], v[90:91], s[70:71] op_sel_hi:[1,0]
	v_pk_mul_f32 v[92:93], v[92:93], s[70:71] op_sel_hi:[1,0]
	v_pk_mul_f32 v[162:163], v[70:71], v[90:91]
	v_pk_mul_f32 v[90:91], v[72:73], v[92:93]
	v_pk_fma_f32 v[92:93], v[152:153], s[62:63], v[162:163] op_sel_hi:[1,0,1]
	v_pk_fma_f32 v[90:91], v[94:95], s[62:63], v[90:91] op_sel_hi:[1,0,1]
	v_cvt_pk_f32_fp8_e32 v[94:95], v143
	v_cvt_pk_f32_fp8_sdwa v[142:143], v143 src0_sel:WORD_1
	v_cvt_pk_f32_fp8_e32 v[152:153], v141
	v_cvt_pk_f32_fp8_sdwa v[140:141], v141 src0_sel:WORD_1
	v_pk_add_f32 v[94:95], v[94:95], 0 op_sel_hi:[1,0]
	v_pk_add_f32 v[142:143], v[142:143], 0 op_sel_hi:[1,0]
	v_pk_add_f32 v[94:95], v[94:95], v[152:153]
	v_pk_add_f32 v[140:141], v[142:143], v[140:141]
	v_cvt_pk_f32_fp8_e32 v[142:143], v145
	v_cvt_pk_f32_fp8_sdwa v[144:145], v145 src0_sel:WORD_1
	v_cvt_pk_f32_fp8_sdwa v[152:153], v98 src0_sel:WORD_1
	v_add_f32_e32 v0, v92, v93
	v_pk_add_f32 v[94:95], v[94:95], v[142:143]
	v_cvt_pk_f32_fp8_e32 v[142:143], v149
	v_pk_add_f32 v[140:141], v[140:141], v[144:145]
	v_cvt_pk_f32_fp8_sdwa v[144:145], v149 src0_sel:WORD_1
	v_cvt_pk_f32_fp8_e32 v[148:149], v98
	v_pk_add_f32 v[94:95], v[94:95], v[142:143]
	v_pk_add_f32 v[140:141], v[140:141], v[144:145]
	v_pk_mul_f32 v[94:95], v[94:95], s[70:71] op_sel_hi:[1,0]
	v_pk_mul_f32 v[140:141], v[140:141], s[70:71] op_sel_hi:[1,0]
	v_pk_mul_f32 v[142:143], v[74:75], v[94:95]
	v_pk_mul_f32 v[94:95], v[76:77], v[140:141]
	v_pk_fma_f32 v[140:141], v[154:155], s[62:63], v[142:143] op_sel_hi:[1,0,1]
	v_cvt_pk_f32_fp8_e32 v[142:143], v100
	v_cvt_pk_f32_fp8_sdwa v[144:145], v100 src0_sel:WORD_1
	v_pk_fma_f32 v[94:95], v[156:157], s[62:63], v[94:95] op_sel_hi:[1,0,1]
	v_pk_add_f32 v[142:143], v[142:143], 0 op_sel_hi:[1,0]
	v_pk_add_f32 v[144:145], v[144:145], 0 op_sel_hi:[1,0]
	v_pk_add_f32 v[142:143], v[142:143], v[148:149]
	v_cvt_pk_f32_fp8_e32 v[148:149], v102
	v_pk_add_f32 v[144:145], v[144:145], v[152:153]
	v_cvt_pk_f32_fp8_sdwa v[152:153], v102 src0_sel:WORD_1
	v_pk_add_f32 v[142:143], v[142:143], v[148:149]
	v_cvt_pk_f32_fp8_e32 v[148:149], v104
	v_pk_add_f32 v[144:145], v[144:145], v[152:153]
	v_cvt_pk_f32_fp8_sdwa v[152:153], v104 src0_sel:WORD_1
	v_pk_add_f32 v[142:143], v[142:143], v[148:149]
	v_cvt_pk_f32_fp8_e32 v[148:149], v101
	v_cvt_pk_f32_fp8_sdwa v[100:101], v101 src0_sel:WORD_1
	v_pk_add_f32 v[144:145], v[144:145], v[152:153]
	v_cvt_pk_f32_fp8_e32 v[152:153], v99
	v_cvt_pk_f32_fp8_sdwa v[98:99], v99 src0_sel:WORD_1
	v_pk_add_f32 v[100:101], v[100:101], 0 op_sel_hi:[1,0]
	v_pk_add_f32 v[148:149], v[148:149], 0 op_sel_hi:[1,0]
	v_pk_mul_f32 v[144:145], v[144:145], s[70:71] op_sel_hi:[1,0]
	v_pk_add_f32 v[98:99], v[100:101], v[98:99]
	v_cvt_pk_f32_fp8_e32 v[100:101], v103
	v_cvt_pk_f32_fp8_sdwa v[102:103], v103 src0_sel:WORD_1
	v_pk_add_f32 v[148:149], v[148:149], v[152:153]
	v_pk_mul_f32 v[142:143], v[142:143], s[70:71] op_sel_hi:[1,0]
	v_pk_add_f32 v[100:101], v[148:149], v[100:101]
	v_pk_add_f32 v[98:99], v[98:99], v[102:103]
	v_cvt_pk_f32_fp8_e32 v[102:103], v105
	v_cvt_pk_f32_fp8_sdwa v[104:105], v105 src0_sel:WORD_1
	v_pk_mul_f32 v[142:143], v[78:79], v[142:143]
	v_pk_mul_f32 v[144:145], v[80:81], v[144:145]
	v_pk_add_f32 v[100:101], v[100:101], v[102:103]
	v_pk_add_f32 v[98:99], v[98:99], v[104:105]
	v_pk_fma_f32 v[144:145], v[160:161], s[62:63], v[144:145] op_sel_hi:[1,0,1]
	v_pk_mul_f32 v[98:99], v[98:99], s[70:71] op_sel_hi:[1,0]
	v_pk_fma_f32 v[142:143], v[158:159], s[62:63], v[142:143] op_sel_hi:[1,0,1]
	v_pk_mul_f32 v[98:99], v[88:89], v[98:99]
	v_pk_mul_f32 v[100:101], v[100:101], s[70:71] op_sel_hi:[1,0]
	v_pk_fma_f32 v[148:149], v[150:151], s[62:63], v[98:99] op_sel_hi:[1,0,1]
	v_add_f32_e32 v98, v90, v91
	v_add_f32_e32 v0, v0, v98
	v_add_f32_e32 v98, v140, v141
	v_add_f32_e32 v99, v94, v95
	v_add_f32_e32 v0, 0, v0
	v_add_f32_e32 v98, v98, v99
	v_pk_mul_f32 v[100:101], v[86:87], v[100:101]
	v_add_f32_e32 v0, v0, v98
	v_add_f32_e32 v98, v142, v143
	v_add_f32_e32 v99, v144, v145
	v_pk_fma_f32 v[96:97], v[96:97], s[62:63], v[100:101] op_sel_hi:[1,0,1]
	v_add_f32_e32 v98, v98, v99
	v_add_f32_e32 v0, v0, v98
	v_add_f32_e32 v98, v96, v97
	v_add_f32_e32 v99, v148, v149
	v_add_f32_e32 v98, v98, v99
	v_add_f32_e32 v0, v0, v98
	ds_swizzle_b32 v98, v0 offset:swizzle(SWAP,1)
	s_waitcnt lgkmcnt(0)
; __device__ __forceinline__ unsigned pk2(float lo, float hi) { return f2bf(lo) | (f2bf(hi) << 16); }
; template <int MODE, bool FIRSTX>
; __device__ __forceinline__ void row_pass(Frame& F, int layer, bool final_out, int row0) {
;     ...
;             const float mean = wave_sum(s) * (1.0f / DM); float qq = 0.f;
; #pragma unroll
;             for (int q = 0; q < 4; ++q) { v[q] = v[q] - mean; qq += (v[q][0] * v[q][0] + v[q][1] * v[q][1]) + (v[q][2] * v[q][2] + v[q][3] * v[q][3]); }
;             const float rstd = 1.0f / sqrtf(wave_sum(qq) * (1.0f / DM) + LN_EPS);
; #pragma unroll
;             for (int q = 0; q < 4; ++q) v[q] = v[q] * rstd * lg[q] + lb[q];
;             if (final_out) { if (row >= NCTX) {
; #pragma unroll
;                 for (int q = 0; q < 4; ++q) *(f32x4*)(F.out + (size_t)(row - NCTX) * DM + RP_COL(q)) = v[q]; } }
;             else {
; #pragma unroll
;                 for (int j = 0; j < 2; ++j) { u32x4 w; w.x = pk2(v[2 * j][0], v[2 * j][1]); w.y = pk2(v[2 * j][2], v[2 * j][3]); w.z = pk2(v[2 * j + 1][0], v[2 * j + 1][1]); w.w = pk2(v[2 * j + 1][2], v[2 * j + 1][3]);
;                     *(u32x4*)(X + (size_t)row * DM + lc + 512 * j) = w; } }
	v_add_f32_e32 v0, v0, v98
	ds_swizzle_b32 v98, v0 offset:swizzle(SWAP,2)
	s_waitcnt lgkmcnt(0)
	v_add_f32_e32 v0, v0, v98
	ds_swizzle_b32 v98, v0 offset:swizzle(SWAP,4)
	s_waitcnt lgkmcnt(0)
	v_add_f32_e32 v0, v0, v98
	ds_swizzle_b32 v98, v0 offset:swizzle(SWAP,8)
	s_waitcnt lgkmcnt(0)
	v_add_f32_e32 v0, v0, v98
	ds_swizzle_b32 v98, v0 offset:swizzle(SWAP,16)
	s_waitcnt lgkmcnt(0)
	v_add_f32_e32 v0, v0, v98
	v_mov_b32_e32 v98, v0
	s_nop 1
	v_permlane32_swap_b32_e32 v0, v98
	v_add_f32_e32 v0, v0, v98
	v_fmac_f32_e32 v91, 0xba800000, v0
	v_fmac_f32_e32 v93, 0xba800000, v0
	v_fmamk_f32 v90, v0, 0xba800000, v90
	v_fmamk_f32 v92, v0, 0xba800000, v92
	v_mul_f32_e32 v98, v93, v93
	v_mul_f32_e32 v99, v91, v91
	v_fmac_f32_e32 v98, v92, v92
	v_fmac_f32_e32 v99, v90, v90
	v_fmac_f32_e32 v95, 0xba800000, v0
	v_fmac_f32_e32 v141, 0xba800000, v0
	v_add_f32_e32 v98, v98, v99
	v_fmamk_f32 v94, v0, 0xba800000, v94
	v_fmamk_f32 v140, v0, 0xba800000, v140
	v_mul_f32_e32 v99, v141, v141
	v_mul_f32_e32 v100, v95, v95
	v_fmac_f32_e32 v99, v140, v140
	v_fmac_f32_e32 v100, v94, v94
	v_add_f32_e32 v99, v99, v100
	v_fmac_f32_e32 v145, 0xba800000, v0
	v_fmac_f32_e32 v143, 0xba800000, v0
	v_add_f32_e32 v98, v98, v99
	v_fmamk_f32 v144, v0, 0xba800000, v144
	v_fmamk_f32 v142, v0, 0xba800000, v142
	v_mul_f32_e32 v99, v143, v143
	v_mul_f32_e32 v100, v145, v145
	v_fmac_f32_e32 v99, v142, v142
	v_fmac_f32_e32 v100, v144, v144
	v_add_f32_e32 v99, v99, v100
	v_fmac_f32_e32 v149, 0xba800000, v0
	v_fmac_f32_e32 v97, 0xba800000, v0
	v_add_f32_e32 v98, v99, v98
	v_fmamk_f32 v148, v0, 0xba800000, v148
	v_fmamk_f32 v96, v0, 0xba800000, v96
	v_mul_f32_e32 v0, v97, v97
	v_mul_f32_e32 v99, v149, v149
	v_fmac_f32_e32 v0, v96, v96
	v_fmac_f32_e32 v99, v148, v148
	v_add_f32_e32 v0, v0, v99
	v_add_f32_e32 v0, v0, v98
	ds_swizzle_b32 v98, v0 offset:swizzle(SWAP,1)
	s_waitcnt lgkmcnt(0)
	v_add_f32_e32 v0, v0, v98
	ds_swizzle_b32 v98, v0 offset:swizzle(SWAP,2)
	s_waitcnt lgkmcnt(0)
	v_add_f32_e32 v0, v0, v98
	ds_swizzle_b32 v98, v0 offset:swizzle(SWAP,4)
	s_waitcnt lgkmcnt(0)
	v_add_f32_e32 v0, v0, v98
	ds_swizzle_b32 v98, v0 offset:swizzle(SWAP,8)
	s_waitcnt lgkmcnt(0)
	v_add_f32_e32 v0, v0, v98
	ds_swizzle_b32 v98, v0 offset:swizzle(SWAP,16)
	s_waitcnt lgkmcnt(0)
	v_add_f32_e32 v0, v0, v98
	v_mov_b32_e32 v98, v0
	s_nop 1
	v_permlane32_swap_b32_e32 v0, v98
	v_add_f32_e32 v0, v0, v98
	v_fmamk_f32 v0, v0, 0x3a800000, v188
	v_cmp_gt_f32_e32 vcc, s31, v0
	v_mul_f32_e32 v98, 0x4f800000, v0
	s_nop 0
	v_cndmask_b32_e32 v0, v0, v98, vcc
	v_sqrt_f32_e32 v98, v0
	s_nop 0
	v_add_u32_e32 v99, -1, v98
	v_fma_f32 v100, -v99, v98, v0
	v_cmp_ge_f32_e64 s[4:5], 0, v100
	v_add_u32_e32 v100, 1, v98
	s_nop 0
	v_cndmask_b32_e64 v99, v98, v99, s[4:5]
	v_fma_f32 v98, -v100, v98, v0
	v_cmp_lt_f32_e64 s[4:5], 0, v98
	s_nop 1
	v_cndmask_b32_e64 v98, v99, v100, s[4:5]
	v_mul_f32_e32 v99, 0x37800000, v98
	v_cndmask_b32_e32 v98, v98, v99, vcc
	v_cmp_class_f32_e32 vcc, v0, v189
	s_nop 1
	v_cndmask_b32_e32 v0, v98, v0, vcc
	v_div_scale_f32 v98, s[0:1], v0, v0, 1.0
	v_rcp_f32_e32 v99, v98
	s_mov_b64 s[0:1], -1
	v_fma_f32 v100, -v98, v99, 1.0
	v_fmac_f32_e32 v99, v100, v99
	v_div_scale_f32 v100, vcc, 1.0, v0, 1.0
	v_mul_f32_e32 v101, v100, v99
	v_fma_f32 v102, -v98, v101, v100
	v_fmac_f32_e32 v101, v102, v99
	v_fma_f32 v98, -v98, v101, v100
	v_div_fmas_f32 v98, v98, v99, v101
	v_div_fixup_f32 v0, v98, v0, 1.0
	v_pk_mul_f32 v[92:93], v[92:93], v[0:1] op_sel_hi:[1,0]
	v_pk_mul_f32 v[90:91], v[90:91], v[0:1] op_sel_hi:[1,0]
	v_pk_fma_f32 v[98:99], v[2:3], v[92:93], v[6:7]
	v_pk_fma_f32 v[100:101], v[4:5], v[90:91], v[8:9]
	v_pk_mul_f32 v[90:91], v[140:141], v[0:1] op_sel_hi:[1,0]
	v_pk_mul_f32 v[92:93], v[94:95], v[0:1] op_sel_hi:[1,0]
	v_pk_fma_f32 v[102:103], v[10:11], v[90:91], v[14:15]
	v_pk_fma_f32 v[104:105], v[12:13], v[92:93], v[16:17]
	v_pk_mul_f32 v[90:91], v[142:143], v[0:1] op_sel_hi:[1,0]
	v_pk_mul_f32 v[92:93], v[144:145], v[0:1] op_sel_hi:[1,0]
	v_pk_mul_f32 v[94:95], v[96:97], v[0:1] op_sel_hi:[1,0]
	v_pk_mul_f32 v[96:97], v[148:149], v[0:1] op_sel_hi:[1,0]
	v_pk_fma_f32 v[92:93], v[20:21], v[92:93], v[24:25]
	v_pk_fma_f32 v[90:91], v[18:19], v[90:91], v[22:23]
	v_pk_fma_f32 v[96:97], v[28:29], v[96:97], v[32:33]
	v_pk_fma_f32 v[94:95], v[26:27], v[94:95], v[30:31]
	s_waitcnt vmcnt(0)
	s_and_b64 vcc, exec, s[2:3]
	s_cbranch_vccnz .LBB0_1212
	v_bfe_u32 v0, v98, 16, 1
	v_add3_u32 v0, v98, v0, s43
	v_bfe_u32 v107, v99, 16, 1
	v_lshrrev_b32_e32 v0, 16, v0
	v_add3_u32 v107, v99, v107, s43
	v_and_or_b32 v140, v107, s33, v0
	v_bfe_u32 v0, v100, 16, 1
	v_add3_u32 v0, v100, v0, s43
	v_bfe_u32 v107, v101, 16, 1
	v_lshrrev_b32_e32 v0, 16, v0
	v_add3_u32 v107, v101, v107, s43
	v_and_or_b32 v141, v107, s33, v0
	v_bfe_u32 v0, v102, 16, 1
	v_add3_u32 v0, v102, v0, s43
	v_bfe_u32 v107, v103, 16, 1
	v_lshrrev_b32_e32 v0, 16, v0
	v_add3_u32 v107, v103, v107, s43
	v_and_or_b32 v142, v107, s33, v0
	v_bfe_u32 v0, v104, 16, 1
	v_add3_u32 v0, v104, v0, s43
	v_bfe_u32 v107, v105, 16, 1
	v_lshrrev_b32_e32 v0, 16, v0
	v_add3_u32 v107, v105, v107, s43
	v_and_or_b32 v143, v107, s33, v0
	v_bfe_u32 v0, v90, 16, 1
	v_add_co_u32_e32 v144, vcc, s39, v138
	v_add3_u32 v0, v90, v0, s43
	v_bfe_u32 v107, v91, 16, 1
	v_addc_co_u32_e32 v145, vcc, 0, v139, vcc
	v_lshrrev_b32_e32 v0, 16, v0
	v_add3_u32 v107, v91, v107, s43
	global_store_dwordx4 v[144:145], v[140:143], off
	s_mov_b64 s[0:1], 0
	s_nop 0
	v_and_or_b32 v140, v107, s33, v0
	v_bfe_u32 v0, v92, 16, 1
	v_add3_u32 v0, v92, v0, s43
	v_bfe_u32 v107, v93, 16, 1
	v_lshrrev_b32_e32 v0, 16, v0
	v_add3_u32 v107, v93, v107, s43
	v_and_or_b32 v141, v107, s33, v0
	v_bfe_u32 v0, v94, 16, 1
	v_add3_u32 v0, v94, v0, s43
	v_bfe_u32 v107, v95, 16, 1
	v_lshrrev_b32_e32 v0, 16, v0
	v_add3_u32 v107, v95, v107, s43
	v_and_or_b32 v142, v107, s33, v0
	v_bfe_u32 v0, v96, 16, 1
	v_add3_u32 v0, v96, v0, s43
	v_bfe_u32 v107, v97, 16, 1
	v_lshrrev_b32_e32 v0, 16, v0
	v_add3_u32 v107, v97, v107, s43
	v_and_or_b32 v143, v107, s33, v0
	global_store_dwordx4 v[144:145], v[140:143], off offset:1024
